# v10 + rows2 log-forget reduce_scatter via permlane32/16 swaps and DPP (exact, replaces ds_bpermute chains)
# speedup vs baseline: 1.0070x; 1.0020x over previous
.LBB0_1574:
	s_andn2_b64 vcc, exec, s[0:1]
	s_cbranch_vccnz .LBB0_1569
	ds_read_b128 v[42:45], v244 offset:4096
	ds_read_b128 v[46:49], v244 offset:5120
	ds_read_b128 v[50:53], v244 offset:6144
	ds_read_b128 v[54:57], v244 offset:7168
	s_waitcnt lgkmcnt(3)
	v_pk_fma_f32 v[58:59], v[90:91], v[42:43], 0 op_sel_hi:[1,1,0]
	s_nop 0
	v_pk_fma_f32 v[58:59], v[92:93], v[44:45], v[58:59]
	s_waitcnt lgkmcnt(2)
	v_pk_fma_f32 v[58:59], v[110:111], v[46:47], v[58:59]
	s_nop 0
	v_pk_fma_f32 v[58:59], v[112:113], v[48:49], v[58:59]
	s_waitcnt lgkmcnt(1)
	v_pk_fma_f32 v[58:59], v[130:131], v[50:51], v[58:59]
	s_nop 0
	v_pk_fma_f32 v[58:59], v[132:133], v[52:53], v[58:59]
	s_waitcnt lgkmcnt(0)
	v_pk_fma_f32 v[62:63], v[142:143], v[54:55], v[58:59]
	ds_read_b128 v[58:61], v244 offset:9232
	ds_read_b128 v[70:73], v244 offset:8208
	v_pk_fma_f32 v[62:63], v[144:145], v[56:57], v[62:63]
	s_waitcnt lgkmcnt(0)
	v_pk_fma_f32 v[74:75], v[90:91], v[70:71], 0 op_sel_hi:[1,1,0]
	v_add_f32_e32 v245, v62, v63
	ds_read_b128 v[62:65], v244 offset:11280
	ds_read_b128 v[66:69], v244 offset:10256
	v_pk_fma_f32 v[74:75], v[92:93], v[72:73], v[74:75]
	ds_read_b128 v[78:81], v244 offset:13344
	ds_read_b128 v[86:89], v244 offset:12320
	v_pk_fma_f32 v[74:75], v[110:111], v[58:59], v[74:75]
	s_waitcnt lgkmcnt(0)
	v_pk_fma_f32 v[94:95], v[90:91], v[86:87], 0 op_sel_hi:[1,1,0]
	v_pk_fma_f32 v[74:75], v[112:113], v[60:61], v[74:75]
	v_pk_fma_f32 v[94:95], v[92:93], v[88:89], v[94:95]
	v_pk_fma_f32 v[74:75], v[130:131], v[66:67], v[74:75]
	v_pk_fma_f32 v[94:95], v[110:111], v[78:79], v[94:95]
	v_pk_fma_f32 v[74:75], v[132:133], v[68:69], v[74:75]
	v_pk_fma_f32 v[94:95], v[112:113], v[80:81], v[94:95]
	v_pk_fma_f32 v[74:75], v[142:143], v[62:63], v[74:75]
	s_nop 0
	v_pk_fma_f32 v[74:75], v[144:145], v[64:65], v[74:75]
	s_nop 0
	v_add_f32_e32 v246, v74, v75
	ds_read_b128 v[74:77], v244 offset:15392
	ds_read_b128 v[82:85], v244 offset:14368
	ds_read_b128 v[98:101], v244 offset:17456
	ds_read_b128 v[106:109], v244 offset:16432
	s_waitcnt lgkmcnt(2)
	v_pk_fma_f32 v[94:95], v[130:131], v[82:83], v[94:95]
	s_nop 0
	v_pk_fma_f32 v[94:95], v[132:133], v[84:85], v[94:95]
	s_waitcnt lgkmcnt(0)
	v_pk_fma_f32 v[114:115], v[90:91], v[106:107], 0 op_sel_hi:[1,1,0]
	v_pk_fma_f32 v[94:95], v[142:143], v[74:75], v[94:95]
	v_pk_fma_f32 v[114:115], v[92:93], v[108:109], v[114:115]
	v_pk_fma_f32 v[94:95], v[144:145], v[76:77], v[94:95]
	v_pk_fma_f32 v[114:115], v[110:111], v[98:99], v[114:115]
	v_add_f32_e32 v247, v94, v95
	ds_read_b128 v[94:97], v244 offset:19504
	ds_read_b128 v[102:105], v244 offset:18480
	v_pk_fma_f32 v[114:115], v[112:113], v[100:101], v[114:115]
	s_waitcnt lgkmcnt(0)
	v_pk_fma_f32 v[114:115], v[130:131], v[102:103], v[114:115]
	s_nop 0
	v_pk_fma_f32 v[114:115], v[132:133], v[104:105], v[114:115]
	s_nop 0
	v_pk_fma_f32 v[114:115], v[142:143], v[94:95], v[114:115]
	s_nop 0
	v_pk_fma_f32 v[114:115], v[144:145], v[96:97], v[114:115]
	s_nop 0
	v_add_f32_e32 v248, v114, v115
	ds_read_b128 v[114:117], v244 offset:20544
	ds_read_b128 v[118:121], v244 offset:21568
	ds_read_b128 v[122:125], v244 offset:22592
	ds_read_b128 v[126:129], v244 offset:23616
	ds_read_b128 v[138:141], v244 offset:25680
	ds_read_b128 v[154:157], v244 offset:24656
	s_waitcnt lgkmcnt(5)
	v_pk_fma_f32 v[134:135], v[90:91], v[114:115], 0 op_sel_hi:[1,1,0]
	ds_read_b128 v[146:149], v244 offset:27728
	ds_read_b128 v[150:153], v244 offset:26704
	v_pk_fma_f32 v[134:135], v[92:93], v[116:117], v[134:135]
	ds_read_b128 v[162:165], v244 offset:29792
	ds_read_b128 v[170:173], v244 offset:28768
	s_waitcnt lgkmcnt(8)
	v_pk_fma_f32 v[134:135], v[110:111], v[118:119], v[134:135]
	ds_read_b128 v[158:161], v244 offset:31840
	ds_read_b128 v[166:169], v244 offset:30816
	v_pk_fma_f32 v[134:135], v[112:113], v[120:121], v[134:135]
	ds_read_b128 v[174:177], v244 offset:33904
	ds_read_b128 v[182:185], v244 offset:32880
	s_waitcnt lgkmcnt(11)
	v_pk_fma_f32 v[134:135], v[130:131], v[122:123], v[134:135]
	s_waitcnt lgkmcnt(0)
	v_pk_fma_f32 v[230:231], v[90:91], v[182:183], 0 op_sel_hi:[1,1,0]
	v_pk_fma_f32 v[134:135], v[132:133], v[124:125], v[134:135]
	v_pk_fma_f32 v[230:231], v[92:93], v[184:185], v[230:231]
	v_pk_fma_f32 v[134:135], v[142:143], v[126:127], v[134:135]
	v_pk_fma_f32 v[230:231], v[110:111], v[174:175], v[230:231]
	v_pk_fma_f32 v[134:135], v[144:145], v[128:129], v[134:135]
	v_pk_fma_f32 v[230:231], v[112:113], v[176:177], v[230:231]
	v_add_f32_e32 v249, v134, v135
	v_pk_fma_f32 v[134:135], v[90:91], v[154:155], 0 op_sel_hi:[1,1,0]
	s_nop 0
	v_pk_fma_f32 v[134:135], v[92:93], v[156:157], v[134:135]
	s_nop 0
	v_pk_fma_f32 v[134:135], v[110:111], v[138:139], v[134:135]
	s_nop 0
	v_pk_fma_f32 v[134:135], v[112:113], v[140:141], v[134:135]
	s_nop 0
	v_pk_fma_f32 v[134:135], v[130:131], v[150:151], v[134:135]
	s_nop 0
	v_pk_fma_f32 v[134:135], v[132:133], v[152:153], v[134:135]
	s_nop 0
	v_pk_fma_f32 v[134:135], v[142:143], v[146:147], v[134:135]
	s_nop 0
	v_pk_fma_f32 v[134:135], v[144:145], v[148:149], v[134:135]
	s_nop 0
	v_add_f32_e32 v250, v134, v135
	v_pk_fma_f32 v[134:135], v[90:91], v[170:171], 0 op_sel_hi:[1,1,0]
	s_nop 0
	v_pk_fma_f32 v[134:135], v[92:93], v[172:173], v[134:135]
	s_nop 0
	v_pk_fma_f32 v[134:135], v[110:111], v[162:163], v[134:135]
	s_nop 0
	v_pk_fma_f32 v[134:135], v[112:113], v[164:165], v[134:135]
	s_nop 0
	v_pk_fma_f32 v[134:135], v[130:131], v[166:167], v[134:135]
	s_nop 0
	v_pk_fma_f32 v[134:135], v[132:133], v[168:169], v[134:135]
	s_nop 0
	v_pk_fma_f32 v[134:135], v[142:143], v[158:159], v[134:135]
	s_nop 0
	v_pk_fma_f32 v[134:135], v[144:145], v[160:161], v[134:135]
	s_nop 0
	v_add_f32_e32 v251, v134, v135
	ds_read_b128 v[134:137], v244 offset:35952
	ds_read_b128 v[178:181], v244 offset:34928
	s_waitcnt lgkmcnt(0)
	v_pk_fma_f32 v[230:231], v[130:131], v[178:179], v[230:231]
	s_nop 0
	v_pk_fma_f32 v[230:231], v[132:133], v[180:181], v[230:231]
	s_nop 0
	v_pk_fma_f32 v[230:231], v[142:143], v[134:135], v[230:231]
	s_nop 0
	v_pk_fma_f32 v[230:231], v[144:145], v[136:137], v[230:231]
	s_nop 0
	v_add_f32_e32 v230, v230, v231
	s_ashr_i32 s51, s50, 31
	s_lshl_b64 s[14:15], s[50:51], 11
	s_add_u32 s14, s29, s14
	s_addc_u32 s15, s33, s15
	v_cvt_pk_bf16_f32 v90, v90, v91
	v_cvt_pk_bf16_f32 v91, v92, v93
	v_lshl_add_u64 v[92:93], v[192:193], 1, s[14:15]
	global_store_dwordx2 v[92:93], v[90:91], off
	v_cvt_pk_bf16_f32 v90, v110, v111
	v_cvt_pk_bf16_f32 v91, v112, v113
	global_store_dwordx2 v[92:93], v[90:91], off offset:512
	v_cvt_pk_bf16_f32 v90, v130, v131
	v_cvt_pk_bf16_f32 v91, v132, v133
	global_store_dwordx2 v[92:93], v[90:91], off offset:1024
	v_cvt_pk_bf16_f32 v90, v142, v143
	v_cvt_pk_bf16_f32 v91, v144, v145
	global_store_dwordx2 v[92:93], v[90:91], off offset:1536
	s_nop 1
	v_permlane32_swap_b32_e32 v245, v249
	v_permlane32_swap_b32_e32 v246, v250
	v_permlane32_swap_b32_e32 v247, v251
	v_permlane32_swap_b32_e32 v248, v230
	v_add_f32_e32 v90, v245, v249
	v_add_f32_e32 v91, v246, v250
	v_add_f32_e32 v92, v247, v251
	v_add_f32_e32 v93, v248, v230
	s_nop 1
	v_permlane16_swap_b32_e32 v90, v92
	v_permlane16_swap_b32_e32 v91, v93
	v_add_f32_e32 v90, v90, v92
	v_add_f32_e32 v91, v91, v93
	s_nop 0
	v_cndmask_b32_e64 v92, v90, v91, s[42:43]
	s_nop 1
	v_mov_b32_dpp v92, v92 row_ror:8 row_mask:0xf bank_mask:0xf
	v_cndmask_b32_e64 v90, v91, v90, s[42:43]
	s_waitcnt lgkmcnt(0)
	v_add_f32_e32 v90, v90, v92
	s_nop 1
	v_mov_b32_dpp v91, v90 row_half_mirror row_mask:0xf bank_mask:0xf
	s_nop 1
	v_mov_b32_dpp v91, v91 quad_perm:[3,2,1,0] row_mask:0xf bank_mask:0xf
	s_waitcnt lgkmcnt(0)
	v_add_f32_e32 v90, v90, v91
	s_nop 1
	v_mov_b32_dpp v91, v90 quad_perm:[2,3,0,1] row_mask:0xf bank_mask:0xf
	s_waitcnt lgkmcnt(0)
	v_add_f32_e32 v90, v90, v91
	s_nop 1
	v_mov_b32_dpp v91, v90 quad_perm:[1,0,3,2] row_mask:0xf bank_mask:0xf
	s_and_saveexec_b64 s[14:15], s[44:45]
	s_cbranch_execz .LBB0_1577
	global_load_dword v92, v[200:201], off
	s_waitcnt lgkmcnt(0)
	v_add_f32_e32 v90, v90, v91
	s_mov_b32 s25, 0xbfb8aa3b
	s_lshr_b32 s2, s51, 20
	s_add_i32 s2, s50, s2
	s_ashr_i32 s24, s2, 12
	s_and_b32 s2, s2, 0xfffff000
	s_sub_i32 s34, s50, s2
	s_ashr_i32 s35, s34, 31
	s_waitcnt vmcnt(0)
	v_add_f32_e32 v92, v90, v92
	v_mul_f32_e64 v90, |v92|, s25
	v_exp_f32_e32 v90, v90
	s_ashr_i32 s25, s24, 31
	s_lshl_b64 s[24:25], s[24:25], 17
	v_min_f32_e32 v92, 0, v92
	v_add_f32_e32 v90, 1.0, v90
	v_log_f32_e32 v93, v90
	v_lshl_add_u64 v[90:91], v[202:203], 0, s[24:25]
	v_lshl_add_u64 v[90:91], s[34:35], 2, v[90:91]
	v_fmac_f32_e32 v92, 0xbf317218, v93
	global_store_dword v[90:91], v92, off
.LBB0_1577:
	s_or_b64 exec, exec, s[14:15]
	v_pk_fma_f32 v[42:43], v[26:27], v[42:43], 0 op_sel_hi:[1,1,0]
	s_add_i32 s14, s50, 1
	v_pk_fma_f32 v[42:43], v[28:29], v[44:45], v[42:43]
	s_ashr_i32 s15, s14, 31
	v_pk_fma_f32 v[42:43], v[30:31], v[46:47], v[42:43]
	s_lshl_b64 s[24:25], s[14:15], 11
	v_pk_fma_f32 v[42:43], v[32:33], v[48:49], v[42:43]
	s_add_u32 s24, s29, s24
	v_pk_fma_f32 v[42:43], v[34:35], v[50:51], v[42:43]
	s_addc_u32 s25, s33, s25
	v_pk_fma_f32 v[42:43], v[36:37], v[52:53], v[42:43]
	s_nop 0
	v_pk_fma_f32 v[42:43], v[38:39], v[54:55], v[42:43]
	s_nop 0
	v_pk_fma_f32 v[42:43], v[40:41], v[56:57], v[42:43]
	s_nop 0
	v_add_f32_e32 v44, v42, v43
	v_pk_fma_f32 v[42:43], v[26:27], v[70:71], 0 op_sel_hi:[1,1,0]
	s_nop 0
	v_pk_fma_f32 v[42:43], v[28:29], v[72:73], v[42:43]
	s_nop 0
	v_pk_fma_f32 v[42:43], v[30:31], v[58:59], v[42:43]
	s_nop 0
	v_pk_fma_f32 v[42:43], v[32:33], v[60:61], v[42:43]
	s_nop 0
	v_pk_fma_f32 v[42:43], v[34:35], v[66:67], v[42:43]
	s_nop 0
	v_pk_fma_f32 v[42:43], v[36:37], v[68:69], v[42:43]
	s_nop 0
	v_pk_fma_f32 v[42:43], v[38:39], v[62:63], v[42:43]
	s_nop 0
	v_pk_fma_f32 v[42:43], v[40:41], v[64:65], v[42:43]
	s_nop 0
	v_add_f32_e32 v45, v42, v43
	v_pk_fma_f32 v[42:43], v[26:27], v[86:87], 0 op_sel_hi:[1,1,0]
	s_nop 0
	v_pk_fma_f32 v[42:43], v[28:29], v[88:89], v[42:43]
	s_nop 0
	v_pk_fma_f32 v[42:43], v[30:31], v[78:79], v[42:43]
	s_nop 0
	v_pk_fma_f32 v[42:43], v[32:33], v[80:81], v[42:43]
	s_nop 0
	v_pk_fma_f32 v[42:43], v[34:35], v[82:83], v[42:43]
	s_nop 0
	v_pk_fma_f32 v[42:43], v[36:37], v[84:85], v[42:43]
	s_nop 0
	v_pk_fma_f32 v[42:43], v[38:39], v[74:75], v[42:43]
	s_nop 0
	v_pk_fma_f32 v[42:43], v[40:41], v[76:77], v[42:43]
	s_nop 0
	v_add_f32_e32 v46, v42, v43
	v_pk_fma_f32 v[42:43], v[26:27], v[106:107], 0 op_sel_hi:[1,1,0]
	s_nop 0
	v_pk_fma_f32 v[42:43], v[28:29], v[108:109], v[42:43]
	s_nop 0
	v_pk_fma_f32 v[42:43], v[30:31], v[98:99], v[42:43]
	s_nop 0
	v_pk_fma_f32 v[42:43], v[32:33], v[100:101], v[42:43]
	s_nop 0
	v_pk_fma_f32 v[42:43], v[34:35], v[102:103], v[42:43]
	s_nop 0
	v_pk_fma_f32 v[42:43], v[36:37], v[104:105], v[42:43]
	s_nop 0
	v_pk_fma_f32 v[42:43], v[38:39], v[94:95], v[42:43]
	s_nop 0
	v_pk_fma_f32 v[42:43], v[40:41], v[96:97], v[42:43]
	s_nop 0
	v_add_f32_e32 v47, v42, v43
	v_pk_fma_f32 v[42:43], v[26:27], v[114:115], 0 op_sel_hi:[1,1,0]
	s_nop 0
	v_pk_fma_f32 v[42:43], v[28:29], v[116:117], v[42:43]
	s_nop 0
	v_pk_fma_f32 v[42:43], v[30:31], v[118:119], v[42:43]
	s_nop 0
	v_pk_fma_f32 v[42:43], v[32:33], v[120:121], v[42:43]
	s_nop 0
	v_pk_fma_f32 v[42:43], v[34:35], v[122:123], v[42:43]
	s_nop 0
	v_pk_fma_f32 v[42:43], v[36:37], v[124:125], v[42:43]
	s_nop 0
	v_pk_fma_f32 v[42:43], v[38:39], v[126:127], v[42:43]
	s_nop 0
	v_pk_fma_f32 v[42:43], v[40:41], v[128:129], v[42:43]
	s_nop 0
	v_add_f32_e32 v48, v42, v43
	v_pk_fma_f32 v[42:43], v[26:27], v[154:155], 0 op_sel_hi:[1,1,0]
	s_nop 0
	v_pk_fma_f32 v[42:43], v[28:29], v[156:157], v[42:43]
	s_nop 0
	v_pk_fma_f32 v[42:43], v[30:31], v[138:139], v[42:43]
	s_nop 0
	v_pk_fma_f32 v[42:43], v[32:33], v[140:141], v[42:43]
	s_nop 0
	v_pk_fma_f32 v[42:43], v[34:35], v[150:151], v[42:43]
	s_nop 0
	v_pk_fma_f32 v[42:43], v[36:37], v[152:153], v[42:43]
	s_nop 0
	v_pk_fma_f32 v[42:43], v[38:39], v[146:147], v[42:43]
	s_nop 0
	v_pk_fma_f32 v[42:43], v[40:41], v[148:149], v[42:43]
	s_nop 0
	v_add_f32_e32 v49, v42, v43
	v_pk_fma_f32 v[42:43], v[26:27], v[170:171], 0 op_sel_hi:[1,1,0]
	s_nop 0
	v_pk_fma_f32 v[42:43], v[28:29], v[172:173], v[42:43]
	s_nop 0
	v_pk_fma_f32 v[42:43], v[30:31], v[162:163], v[42:43]
	s_nop 0
	v_pk_fma_f32 v[42:43], v[32:33], v[164:165], v[42:43]
	s_nop 0
	v_pk_fma_f32 v[42:43], v[34:35], v[166:167], v[42:43]
	s_nop 0
	v_pk_fma_f32 v[42:43], v[36:37], v[168:169], v[42:43]
	s_nop 0
	v_pk_fma_f32 v[42:43], v[38:39], v[158:159], v[42:43]
	s_nop 0
	v_pk_fma_f32 v[42:43], v[40:41], v[160:161], v[42:43]
	s_nop 0
	v_add_f32_e32 v50, v42, v43
	v_pk_fma_f32 v[42:43], v[26:27], v[182:183], 0 op_sel_hi:[1,1,0]
	v_cvt_pk_bf16_f32 v26, v26, v27
	v_cvt_pk_bf16_f32 v27, v28, v29
	s_nop 0
	v_pk_fma_f32 v[42:43], v[28:29], v[184:185], v[42:43]
	v_lshl_add_u64 v[28:29], v[192:193], 1, s[24:25]
	v_pk_fma_f32 v[42:43], v[30:31], v[174:175], v[42:43]
	global_store_dwordx2 v[28:29], v[26:27], off
	v_cvt_pk_bf16_f32 v26, v30, v31
	v_pk_fma_f32 v[42:43], v[32:33], v[176:177], v[42:43]
	v_cvt_pk_bf16_f32 v27, v32, v33
	global_store_dwordx2 v[28:29], v[26:27], off offset:512
	v_cvt_pk_bf16_f32 v26, v34, v35
	v_pk_fma_f32 v[42:43], v[34:35], v[178:179], v[42:43]
	v_cvt_pk_bf16_f32 v27, v36, v37
	global_store_dwordx2 v[28:29], v[26:27], off offset:1024
	v_cvt_pk_bf16_f32 v26, v38, v39
	v_pk_fma_f32 v[42:43], v[36:37], v[180:181], v[42:43]
	v_cvt_pk_bf16_f32 v27, v40, v41
	global_store_dwordx2 v[28:29], v[26:27], off offset:1536
	s_nop 0
	v_pk_fma_f32 v[26:27], v[38:39], v[134:135], v[42:43]
	v_permlane32_swap_b32_e32 v44, v48
	v_pk_fma_f32 v[26:27], v[40:41], v[136:137], v[26:27]
	v_permlane32_swap_b32_e32 v45, v49
	v_add_f32_e32 v26, v26, v27
	v_permlane32_swap_b32_e32 v46, v50
	s_nop 1
	v_permlane32_swap_b32_e32 v47, v26
	v_add_f32_e32 v27, v44, v48
	v_add_f32_e32 v28, v45, v49
	v_add_f32_e32 v29, v46, v50
	v_add_f32_e32 v26, v47, v26
	s_nop 1
	v_permlane16_swap_b32_e32 v27, v29
	v_permlane16_swap_b32_e32 v28, v26
	v_add_f32_e32 v27, v27, v29
	v_add_f32_e32 v26, v28, v26
	s_nop 0
	v_cndmask_b32_e64 v28, v27, v26, s[42:43]
	s_nop 1
	v_mov_b32_dpp v28, v28 row_ror:8 row_mask:0xf bank_mask:0xf
	v_cndmask_b32_e64 v26, v26, v27, s[42:43]
	s_waitcnt lgkmcnt(0)
	v_add_f32_e32 v26, v26, v28
	s_nop 1
	v_mov_b32_dpp v27, v26 row_half_mirror row_mask:0xf bank_mask:0xf
	s_nop 1
	v_mov_b32_dpp v27, v27 quad_perm:[3,2,1,0] row_mask:0xf bank_mask:0xf
	s_waitcnt lgkmcnt(0)
	v_add_f32_e32 v26, v26, v27
	s_nop 1
	v_mov_b32_dpp v27, v26 quad_perm:[2,3,0,1] row_mask:0xf bank_mask:0xf
	s_waitcnt lgkmcnt(0)
	v_add_f32_e32 v26, v26, v27
	s_nop 1
	v_mov_b32_dpp v27, v26 quad_perm:[1,0,3,2] row_mask:0xf bank_mask:0xf
	s_and_saveexec_b64 s[24:25], s[44:45]
	s_cbranch_execz .LBB0_1568
	global_load_dword v28, v[200:201], off
	s_waitcnt lgkmcnt(0)
	v_add_f32_e32 v26, v26, v27
	s_lshr_b32 s2, s15, 20
	s_mov_b32 s15, 0xbfb8aa3b
	s_add_i32 s2, s14, s2
	s_ashr_i32 s34, s2, 12
	s_and_b32 s2, s2, 0xfffff000
	s_ashr_i32 s35, s34, 31
	s_sub_i32 s14, s14, s2
	s_lshl_b64 s[34:35], s[34:35], 17
	s_waitcnt vmcnt(0)
	v_add_f32_e32 v28, v26, v28
	v_mul_f32_e64 v26, |v28|, s15
	v_exp_f32_e32 v26, v26
	s_ashr_i32 s15, s14, 31
	v_min_f32_e32 v28, 0, v28
	v_add_f32_e32 v26, 1.0, v26
	v_log_f32_e32 v29, v26
	v_lshl_add_u64 v[26:27], v[202:203], 0, s[34:35]
	v_lshl_add_u64 v[26:27], s[14:15], 2, v[26:27]
	v_fmac_f32_e32 v28, 0xbf317218, v29
	global_store_dword v[26:27], v28, off
	s_branch .LBB0_1568
